# v50 + NSA unit prologue de-serialised: first compressed-branch K/V LDS-DMA issued before the wait on the query/gate loads, gate sigmoid math moved behind the DMA issue
# speedup vs baseline: 1.0029x; 1.0029x over previous
.LBB0_1646:
	s_bfe_u32 s3, s5, 0x50001
	s_ashr_i32 s10, s5, 8
	s_bfe_u32 s1, s5, 0x20006
	s_and_b32 s4, s5, 1
	s_xor_b32 s6, s3, 63
	s_cmp_eq_u32 s4, 0
	v_writelane_b32 v255, s5, 6
	s_cselect_b64 s[4:5], -1, 0
	v_writelane_b32 v255, s4, 7
	v_mov_b32_e32 v153, v3
	v_readlane_b32 s8, v254, 20
	v_writelane_b32 v255, s5, 8
	s_and_b64 s[4:5], s[4:5], exec
	s_cselect_b32 s89, s6, s3
	s_lshl_b32 s3, s1, 2
	v_writelane_b32 v255, s3, 9
	v_or_b32_e32 v6, s3, v158
	s_lshl_b32 s3, s89, 6
	s_ashr_i32 s11, s10, 31
	v_writelane_b32 v255, s3, 10
	v_add_u32_e32 v152, s3, v157
	s_lshl_b64 s[4:5], s[10:11], 12
	v_writelane_b32 v255, s4, 11
	s_movk_i32 s3, 0x6a00
	v_lshlrev_b32_e32 v2, 8, v6
	v_lshl_add_u64 v[0:1], s[4:5], 0, v[152:153]
	v_writelane_b32 v255, s5, 12
	v_mad_u64_u32 v[4:5], s[4:5], v0, s3, v[148:149]
	v_mad_i32_i24 v5, v1, s3, v5
	v_lshl_add_u64 v[0:1], v[4:5], 0, v[2:3]
	v_lshl_add_u64 v[0:1], v[144:145], 1, v[0:1]
	global_load_dwordx4 v[136:139], v[0:1], off
	global_load_dwordx4 v[112:115], v[0:1], off offset:32
	global_load_dwordx4 v[116:119], v[0:1], off offset:64
	global_load_dwordx4 v[124:127], v[0:1], off offset:96
	global_load_dwordx4 v[140:143], v[0:1], off offset:128
	global_load_dwordx4 v[132:135], v[0:1], off offset:160
	global_load_dwordx4 v[120:123], v[0:1], off offset:192
	global_load_dwordx4 v[128:131], v[0:1], off offset:224
	v_mul_u32_u24_e32 v0, 3, v6
	v_lshlrev_b32_e32 v2, 1, v0
	v_lshl_add_u64 v[0:1], v[4:5], 0, v[2:3]
	s_mov_b64 s[4:5], 0x6800
	s_movk_i32 s3, 0x6000
	v_lshl_add_u64 v[4:5], v[0:1], 0, s[4:5]
	v_add_co_u32_e32 v0, vcc, s3, v0
	global_load_ushort v212, v[4:5], off offset:4
	s_nop 0
	v_addc_co_u32_e32 v1, vcc, 0, v1, vcc
	global_load_dword v213, v[0:1], off offset:2048
	v_cmp_lt_u32_e32 vcc, 30, v152
	s_lshl_b32 s3, s10, 2
	s_lshl_b32 s4, s89, 2
	s_or_b32 s6, s3, s1
	s_addk_i32 s4, 0x42
	s_ashr_i32 s7, s6, 31
	s_lshr_b32 s5, s4, 6
	s_lshl_b64 s[6:7], s[6:7], 16
	v_readlane_b32 s3, v254, 22
	s_add_u32 s92, s3, s6
	v_readlane_b32 s3, v254, 23
	s_addc_u32 s3, s3, s7
	s_add_u32 s12, s8, s6
	v_readlane_b32 s6, v254, 21
	s_addc_u32 s6, s6, s7
	s_and_b32 s93, s3, 0xffff
	s_mov_b32 s52, s92
	s_mov_b32 s53, s93
	s_mov_b32 m0, s42
	s_and_b32 s13, s6, 0xffff
	s_mov_b32 s14, s54
	s_mov_b32 s15, s55
	s_add_i32 s18, s5, -2
	v_mov_b32_e32 v171, 0xf149f2ca
	s_mov_b32 s3, 0x8000
	v_mov_b32_e32 v46, v3
	v_mov_b32_e32 v44, 0xf149f2ca
	s_mov_b32 s6, s90
	v_add_u32_e32 v0, -15, v152
	v_lshrrev_b32_e32 v0, 4, v0
	v_cndmask_b32_e32 v170, 0, v0, vcc
	v_mbcnt_lo_u32_b32 v2, -1, 0
	v_mbcnt_hi_u32_b32 v2, -1, v2
	v_mov_b32_e32 v43, v170
	v_lshlrev_b32_e32 v4, 4, v2
	v_bfe_u32 v0, v2, 2, 2
	v_lshrrev_b32_e32 v1, 1, v2
	v_add_u32_e32 v6, s40, v4
	v_and_b32_e32 v7, 15, v2
	v_and_or_b32 v8, v1, 8, v0
	v_lshrrev_b32_e32 v0, 4, v2
	v_bitop3_b32 v0, v0, v7, 7 bitop3:0x6c
	v_and_b32_e32 v1, 0xffffff00, v6
	v_lshl_or_b32 v0, v0, 4, v1
	v_ashrrev_i32_e32 v1, 8, v6
	v_and_b32_e32 v10, 0xfffff0, v1
	v_lshrrev_b32_e32 v1, 1, v1
	v_and_b32_e32 v1, 4, v1
	v_or3_b32 v1, v10, v1, v8
	v_lshlrev_b32_e32 v10, 1, v2
	v_and_b32_e32 v9, 48, v4
	v_and_b32_e32 v10, 0xc0, v10
	v_lshlrev_b32_e32 v1, 8, v1
	v_add_u32_e32 v6, 0x400, v6
	v_or3_b32 v1, v1, v10, v9
	v_lshrrev_b32_e32 v10, 8, v6
	v_bitop3_b32 v7, v10, v7, 7 bitop3:0x6c
	v_and_b32_e32 v10, 0xffffff00, v6
	v_lshl_or_b32 v36, v7, 4, v10
	v_ashrrev_i32_e32 v7, 8, v6
	v_and_b32_e32 v10, 0xfffff0, v7
	v_lshrrev_b32_e32 v7, 1, v7
	v_and_b32_e32 v7, 4, v7
	v_or3_b32 v7, v10, v7, v8
	v_lshrrev_b32_e32 v6, 3, v6
	buffer_load_dwordx4 v0, s[52:55], 0 offen lds
	s_mov_b32 m0, s41
	v_and_b32_e32 v6, 0xc0, v6
	v_lshlrev_b32_e32 v7, 8, v7
	buffer_load_dwordx4 v1, s[12:15], 0 offen lds
	s_mov_b32 m0, s43
	v_or3_b32 v37, v7, v6, v9
	buffer_load_dwordx4 v36, s[52:55], 0 offen lds
	s_mov_b32 m0, s44
	v_lshrrev_b32_e32 v5, 5, v2
	buffer_load_dwordx4 v37, s[12:15], 0 offen lds
	v_xor_b32_e32 v5, v5, v2
	v_and_b32_e32 v6, 31, v2
	v_lshlrev_b32_e32 v5, 4, v5
	s_waitcnt vmcnt(4)
	v_lshlrev_b32_e32 v218, 16, v212
	v_mul_f32_e32 v218, 0xbfb8aa3b, v218
	v_exp_f32_e32 v218, v218
	v_lshlrev_b32_e32 v216, 16, v213
	v_and_b32_e32 v217, 0xffff0000, v213
	v_mul_f32_e32 v216, 0xbfb8aa3b, v216
	v_mul_f32_e32 v217, 0xbfb8aa3b, v217
	v_exp_f32_e32 v216, v216
	v_exp_f32_e32 v217, v217
	v_add_f32_e32 v218, 1.0, v218
	v_rcp_f32_e32 v218, v218
	v_add_f32_e32 v216, 1.0, v216
	v_add_f32_e32 v217, 1.0, v217
	v_rcp_f32_e32 v216, v216
	v_rcp_f32_e32 v217, v217
	v_mov_b32_e32 v219, 0
	ds_write_b128 v165, v[216:219]
	s_waitcnt vmcnt(0) lgkmcnt(0)
	s_barrier
	v_lshlrev_b32_e32 v6, 8, v6
	v_and_b32_e32 v5, 16, v5
	v_lshrrev_b32_e32 v2, 3, v2
	v_add3_u32 v5, 0, v6, v5
	v_and_b32_e32 v6, 0x60, v4
	v_bitop3_b32 v7, v4, 32, v166 bitop3:0x6c
	v_bitop3_b32 v8, v4, 64, v166 bitop3:0x6c
	v_bitop3_b32 v4, v4, s70, v4 bitop3:0xc
	v_and_b32_e32 v2, 4, v2
	v_sub_u32_e32 v38, 0, v2
	v_add_u32_e32 v39, v5, v6
	v_add_u32_e32 v40, v5, v7
	v_add_u32_e32 v41, v5, v8
	v_add_u32_e32 v42, v5, v4
	s_branch .LBB0_1649
